# MoE K-loops: one static s_setprio 1 for the leading wave half for the whole K-loop, per-segment priority flips removed (on top of the XCD-aware up map)
# speedup vs baseline: 1.0014x; 1.0007x over previous
; #define PG8_STAGE(bufoff, gbase, voff) do { _Pragma("unroll") for (int _i = 0; _i < 2; ++_i) \
;         __builtin_amdgcn_global_load_lds((const unsigned*)((const char*)(gbase) + (voff)[_i]), (PG8_LAS unsigned*)(lds + (bufoff) + ldsw + _i * 8192), 16, 0, 0); } while (0)
; #define PG8_STAGE_G(bufoff, kb, g) do { _Pragma("unroll") for (int _i = 0; _i < 2; ++_i) \
;         __builtin_amdgcn_global_load_lds((const unsigned*)(gA + (size_t)(kb) + (g)[_i]), (PG8_LAS unsigned*)(lds + (bufoff) + ldsw + _i * 8192), 16, 0, 0); } while (0)
; #define PG8_LDA(dst, b, h) do { _Pragma("unroll") for (int m = 0; m < 4; ++m) _Pragma("unroll") for (int k = 0; k < 2; ++k) dst[m][k] = *(const PG8_LAS bf16x8*)(lds + PG8_SA(b, h) + aoff + m * 2048 + k * 1024); } while (0)
; #define PG8_LDB(dst, b, h) do { _Pragma("unroll") for (int n = 0; n < 2; ++n) _Pragma("unroll") for (int k = 0; k < 2; ++k) dst[n][k] = *(const PG8_LAS bf16x8*)(lds + PG8_SB(b, h) + boff + n * 2048 + k * 1024); } while (0)
; #define PG8_MMA(ai, bj, At, Bt) do { __builtin_amdgcn_s_setprio(1); _Pragma("unroll") for (int m = 0; m < 4; ++m) _Pragma("unroll") for (int n = 0; n < 2; ++n) _Pragma("unroll") for (int k = 0; k < 2; ++k) \
;         acc[ai][bj][m][n] = __builtin_amdgcn_mfma_f32_16x16x32_bf16(Bt[n][k], At[m][k], acc[ai][bj][m][n], 0, 0, 0); __builtin_amdgcn_s_setprio(0); } while (0)
; #define PG8_WAIT_V(n) asm volatile("s_waitcnt vmcnt(" #n ")" ::: "memory")
; template <class Epi, class Sched, bool ALIGN_EPI = false, bool SP2 = false, bool GATHER = false, bool HALFM = false>
; __device__ __forceinline__ void gemm_phase(PG8_LAS unsigned char* lds, const int Kdim, const Sched& S, const Epi& E) {
;     ...
;             PG8_LDB(B0, 0, 0); PG8_LDB(B1, 0, 1); PG8_SCHED; PG8_LDA(At, 0, 0); if constexpr (GATHER) PG8_STAGE_G(PG8_SA(1, 1), (size_t)(t + 1) * kstep, gc[1]); else PG8_STAGE(PG8_SA(1, 1), a1 + hstep, voffA);
;             PG8_WAIT_V(8); PG8_WAIT_L(0); PG8_BAR; PG8_MMA(0, 0, At, B0); PG8_MMA(0, 1, At, B1); PG8_BAR; PG8_SCHED;
;             if constexpr (!HALFM) PG8_LDA(At, 0, 1); PG8_STAGE(PG8_SB(0, 0), b2, voffB); PG8_STAGE(PG8_SB(0, 1), b2 + hstep, voffB); if constexpr (GATHER) PG8_STAGE_G(PG8_SA(0, 0), kb2, s0); else PG8_STAGE(PG8_SA(0, 0), a2, voffA);
;             PG8_WAIT_V(8); PG8_WAIT_L(0); PG8_BAR; if constexpr (!HALFM) { PG8_MMA(1, 0, At, B0); PG8_MMA(1, 1, At, B1); } PG8_BAR; PG8_SCHED;
.Lup_unit_nobar:
	s_cmp_eq_u64 s[0:1], 0
	s_cbranch_scc0 .Lup_prio_done
	s_setprio 1
.Lup_prio_done:
.LBB0_1716:
	s_add_u32 s20, s36, s14
	s_addc_u32 s21, s82, s15
	s_add_u32 s24, s14, 0x100
	s_addc_u32 s25, s15, 0
	s_cmpk_eq_i32 s14, 0x700
	s_cselect_b64 vcc, -1, 0
	s_and_b64 s[4:5], vcc, exec
	s_cselect_b32 s5, s41, s21
	s_cselect_b32 s4, s40, s20
	s_cselect_b32 s20, 0, s24
	s_add_i32 s21, 0, 0x10000
	v_add_u32_e32 v161, s21, v170
	s_add_i32 s33, 0, 0x14000
	ds_read_b128 v[136:139], v161
	ds_read_b128 v[140:143], v161 offset:1024
	ds_read_b128 v[144:147], v161 offset:2048
	ds_read_b128 v[182:185], v161 offset:3072
	v_add_u32_e32 v161, s33, v170
	ds_read_b128 v[186:189], v161
	ds_read_b128 v[190:193], v161 offset:1024
	ds_read_b128 v[194:197], v161 offset:2048
	ds_read_b128 v[198:201], v161 offset:3072
	v_cndmask_b32_e32 v2, v148, v163, vcc
	v_cndmask_b32_e32 v153, v152, v167, vcc
	v_cndmask_b32_e32 v160, v150, v166, vcc
	v_cndmask_b32_e32 v155, v154, v168, vcc
	v_lshl_add_u64 v[220:221], v[134:135], 0, s[14:15]
	s_add_i32 m0, s12, 0xc000
	ds_read_b128 v[202:205], v177
	ds_read_b128 v[208:211], v177 offset:1024
	ds_read_b128 v[224:227], v177 offset:2048
	ds_read_b128 v[228:231], v177 offset:3072
	ds_read_b128 v[232:235], v177 offset:4096
	ds_read_b128 v[236:239], v177 offset:5120
	ds_read_b128 v[240:243], v177 offset:6144
	ds_read_b128 v[244:247], v177 offset:7168
	global_load_lds_dwordx4 v[220:221], off
	v_lshl_add_u64 v[220:221], v[132:133], 0, s[14:15]
	s_add_i32 m0, s12, 0xe000
	s_nop 0
	global_load_lds_dwordx4 v[220:221], off
	s_waitcnt vmcnt(8)
	s_waitcnt lgkmcnt(0)
	s_barrier
	s_waitcnt lgkmcnt(0)
	v_mfma_f32_16x16x32_bf16 v[128:131], v[136:139], v[202:205], v[128:131]
	v_mfma_f32_16x16x32_bf16 v[124:127], v[144:147], v[202:205], v[124:127]
	v_mfma_f32_16x16x32_bf16 v[120:123], v[136:139], v[224:227], v[120:123]
	v_mfma_f32_16x16x32_bf16 v[116:119], v[144:147], v[224:227], v[116:119]
	v_mfma_f32_16x16x32_bf16 v[112:115], v[136:139], v[232:235], v[112:115]
	v_mfma_f32_16x16x32_bf16 v[108:111], v[144:147], v[232:235], v[108:111]
	v_mfma_f32_16x16x32_bf16 v[104:107], v[136:139], v[240:243], v[104:107]
	v_mfma_f32_16x16x32_bf16 v[100:103], v[144:147], v[240:243], v[100:103]
	v_mfma_f32_16x16x32_bf16 v[128:131], v[140:143], v[208:211], v[128:131]
	v_mfma_f32_16x16x32_bf16 v[124:127], v[182:185], v[208:211], v[124:127]
	v_mfma_f32_16x16x32_bf16 v[120:123], v[140:143], v[228:231], v[120:123]
	v_mfma_f32_16x16x32_bf16 v[116:119], v[182:185], v[228:231], v[116:119]
	v_mfma_f32_16x16x32_bf16 v[112:115], v[140:143], v[236:239], v[112:115]
	v_mfma_f32_16x16x32_bf16 v[108:111], v[182:185], v[236:239], v[108:111]
	v_mfma_f32_16x16x32_bf16 v[104:107], v[140:143], v[244:247], v[104:107]
	v_mfma_f32_16x16x32_bf16 v[100:103], v[182:185], v[244:247], v[100:103]
	v_mfma_f32_16x16x32_bf16 v[96:99], v[186:189], v[202:205], v[96:99]
	v_mfma_f32_16x16x32_bf16 v[92:95], v[194:197], v[202:205], v[92:95]
	v_mfma_f32_16x16x32_bf16 v[88:91], v[186:189], v[224:227], v[88:91]
	v_mfma_f32_16x16x32_bf16 v[84:87], v[194:197], v[224:227], v[84:87]
	v_mfma_f32_16x16x32_bf16 v[80:83], v[186:189], v[232:235], v[80:83]
	v_mfma_f32_16x16x32_bf16 v[76:79], v[194:197], v[232:235], v[76:79]
	v_mfma_f32_16x16x32_bf16 v[72:75], v[186:189], v[240:243], v[72:75]
	v_mfma_f32_16x16x32_bf16 v[68:71], v[194:197], v[240:243], v[68:71]
	v_mfma_f32_16x16x32_bf16 v[96:99], v[190:193], v[208:211], v[96:99]
	v_mfma_f32_16x16x32_bf16 v[92:95], v[198:201], v[208:211], v[92:95]
	v_mfma_f32_16x16x32_bf16 v[88:91], v[190:193], v[228:231], v[88:91]
	v_mfma_f32_16x16x32_bf16 v[84:87], v[198:201], v[228:231], v[84:87]
	v_mfma_f32_16x16x32_bf16 v[80:83], v[190:193], v[236:239], v[80:83]
	v_mfma_f32_16x16x32_bf16 v[76:79], v[198:201], v[236:239], v[76:79]
	v_mfma_f32_16x16x32_bf16 v[72:75], v[190:193], v[244:247], v[72:75]
	v_mfma_f32_16x16x32_bf16 v[68:71], v[198:201], v[244:247], v[68:71]
	s_barrier
	s_add_i32 s14, s21, s8
	v_lshl_add_u64 v[220:221], s[4:5], 0, v[156:157]
	s_mov_b32 m0, s14
	ds_read_b128 v[202:205], v177 offset:16384
	ds_read_b128 v[208:211], v177 offset:17408
	ds_read_b128 v[224:227], v177 offset:18432
	ds_read_b128 v[228:231], v177 offset:19456
	ds_read_b128 v[232:235], v177 offset:20480
	ds_read_b128 v[236:239], v177 offset:21504
	ds_read_b128 v[240:243], v177 offset:22528
	ds_read_b128 v[244:247], v177 offset:23552
	global_load_lds_dwordx4 v[220:221], off
	s_add_i32 m0, s14, 0x2000
	s_add_u32 s14, s4, 0x40000
	v_lshl_add_u64 v[216:217], s[4:5], 0, v[158:159]
	s_addc_u32 s15, s5, 0
	s_add_i32 s21, s33, s8
	global_load_lds_dwordx4 v[216:217], off
	v_lshl_add_u64 v[218:219], s[14:15], 0, v[156:157]
	s_mov_b32 m0, s21
	v_mov_b32_e32 v161, v3
	global_load_lds_dwordx4 v[218:219], off
	s_add_i32 m0, s21, 0x2000
	v_lshl_add_u64 v[218:219], s[14:15], 0, v[158:159]
	s_add_u32 s14, s78, s20
	global_load_lds_dwordx4 v[218:219], off
	s_addc_u32 s15, s79, 0
	s_mov_b32 m0, s12
	v_lshl_add_u64 v[218:219], s[14:15], 0, v[2:3]
	global_load_lds_dwordx4 v2, s[14:15]
	s_mov_b32 m0, s13
	s_nop 0
	global_load_lds_dwordx4 v160, s[14:15]
	s_waitcnt vmcnt(8)
	s_waitcnt lgkmcnt(0)
	v_lshl_add_u64 v[160:161], s[14:15], 0, v[160:161]
	s_barrier
; #define PG8_STAGE(bufoff, gbase, voff) do { _Pragma("unroll") for (int _i = 0; _i < 2; ++_i) \
;         __builtin_amdgcn_global_load_lds((const unsigned*)((const char*)(gbase) + (voff)[_i]), (PG8_LAS unsigned*)(lds + (bufoff) + ldsw + _i * 8192), 16, 0, 0); } while (0)
; #define PG8_STAGE_G(bufoff, kb, g) do { _Pragma("unroll") for (int _i = 0; _i < 2; ++_i) \
;         __builtin_amdgcn_global_load_lds((const unsigned*)(gA + (size_t)(kb) + (g)[_i]), (PG8_LAS unsigned*)(lds + (bufoff) + ldsw + _i * 8192), 16, 0, 0); } while (0)
; #define PG8_LDA(dst, b, h) do { _Pragma("unroll") for (int m = 0; m < 4; ++m) _Pragma("unroll") for (int k = 0; k < 2; ++k) dst[m][k] = *(const PG8_LAS bf16x8*)(lds + PG8_SA(b, h) + aoff + m * 2048 + k * 1024); } while (0)
; #define PG8_LDB(dst, b, h) do { _Pragma("unroll") for (int n = 0; n < 2; ++n) _Pragma("unroll") for (int k = 0; k < 2; ++k) dst[n][k] = *(const PG8_LAS bf16x8*)(lds + PG8_SB(b, h) + boff + n * 2048 + k * 1024); } while (0)
; #define PG8_MMA(ai, bj, At, Bt) do { __builtin_amdgcn_s_setprio(1); _Pragma("unroll") for (int m = 0; m < 4; ++m) _Pragma("unroll") for (int n = 0; n < 2; ++n) _Pragma("unroll") for (int k = 0; k < 2; ++k) \
;         acc[ai][bj][m][n] = __builtin_amdgcn_mfma_f32_16x16x32_bf16(Bt[n][k], At[m][k], acc[ai][bj][m][n], 0, 0, 0); __builtin_amdgcn_s_setprio(0); } while (0)
; #define PG8_WAIT_V(n) asm volatile("s_waitcnt vmcnt(" #n ")" ::: "memory")
; #define PG8_WAIT_L(n) asm volatile("s_waitcnt lgkmcnt(" #n ")" ::: "memory")
; #define PG8_BAR __builtin_amdgcn_s_barrier()
; #define PG8_SCHED __builtin_amdgcn_sched_barrier(0)
; template <class Epi, class Sched, bool ALIGN_EPI = false, bool SP2 = false, bool GATHER = false, bool HALFM = false>
; __device__ __forceinline__ void gemm_phase(PG8_LAS unsigned char* lds, const int Kdim, const Sched& S, const Epi& E) {
;     ...
;             PG8_WAIT_V(8); PG8_WAIT_L(0); PG8_BAR; if constexpr (!HALFM) { PG8_MMA(1, 0, At, B0); PG8_MMA(1, 1, At, B1); } PG8_BAR; PG8_SCHED;
;             PG8_LDB(B0, 1, 0); PG8_LDB(B1, 1, 1); PG8_SCHED; PG8_LDA(At, 1, 0); if constexpr (GATHER) PG8_STAGE_G(PG8_SA(0, 1), kb2, s1); else PG8_STAGE(PG8_SA(0, 1), a2 + hstep, voffA);
;             PG8_WAIT_V(8); PG8_WAIT_L(0); PG8_BAR; PG8_MMA(0, 0, At, B0); PG8_MMA(0, 1, At, B1); PG8_BAR; PG8_SCHED;
	s_waitcnt lgkmcnt(0)
	v_mfma_f32_16x16x32_bf16 v[64:67], v[136:139], v[202:205], v[64:67]
	v_mfma_f32_16x16x32_bf16 v[60:63], v[144:147], v[202:205], v[60:63]
	v_mfma_f32_16x16x32_bf16 v[56:59], v[136:139], v[224:227], v[56:59]
	v_mfma_f32_16x16x32_bf16 v[52:55], v[144:147], v[224:227], v[52:55]
	v_mfma_f32_16x16x32_bf16 v[48:51], v[136:139], v[232:235], v[48:51]
	v_mfma_f32_16x16x32_bf16 v[44:47], v[144:147], v[232:235], v[44:47]
	v_mfma_f32_16x16x32_bf16 v[40:43], v[136:139], v[240:243], v[40:43]
	v_mfma_f32_16x16x32_bf16 v[36:39], v[144:147], v[240:243], v[36:39]
	v_mfma_f32_16x16x32_bf16 v[64:67], v[140:143], v[208:211], v[64:67]
	v_mfma_f32_16x16x32_bf16 v[60:63], v[182:185], v[208:211], v[60:63]
	v_mfma_f32_16x16x32_bf16 v[56:59], v[140:143], v[228:231], v[56:59]
	v_mfma_f32_16x16x32_bf16 v[52:55], v[182:185], v[228:231], v[52:55]
	v_mfma_f32_16x16x32_bf16 v[48:51], v[140:143], v[236:239], v[48:51]
	v_mfma_f32_16x16x32_bf16 v[44:47], v[182:185], v[236:239], v[44:47]
	v_mfma_f32_16x16x32_bf16 v[40:43], v[140:143], v[244:247], v[40:43]
	v_mfma_f32_16x16x32_bf16 v[36:39], v[182:185], v[244:247], v[36:39]
	v_mfma_f32_16x16x32_bf16 v[32:35], v[186:189], v[202:205], v[32:35]
	v_mfma_f32_16x16x32_bf16 v[28:31], v[194:197], v[202:205], v[28:31]
	v_mfma_f32_16x16x32_bf16 v[24:27], v[186:189], v[224:227], v[24:27]
	v_mfma_f32_16x16x32_bf16 v[20:23], v[194:197], v[224:227], v[20:23]
	v_mfma_f32_16x16x32_bf16 v[16:19], v[186:189], v[232:235], v[16:19]
	v_mfma_f32_16x16x32_bf16 v[12:15], v[194:197], v[232:235], v[12:15]
	v_mfma_f32_16x16x32_bf16 v[8:11], v[186:189], v[240:243], v[8:11]
	v_mfma_f32_16x16x32_bf16 v[4:7], v[194:197], v[240:243], v[4:7]
	v_mfma_f32_16x16x32_bf16 v[32:35], v[190:193], v[208:211], v[32:35]
	v_mfma_f32_16x16x32_bf16 v[28:31], v[198:201], v[208:211], v[28:31]
	v_mfma_f32_16x16x32_bf16 v[24:27], v[190:193], v[228:231], v[24:27]
	v_mfma_f32_16x16x32_bf16 v[20:23], v[198:201], v[228:231], v[20:23]
	v_mfma_f32_16x16x32_bf16 v[16:19], v[190:193], v[236:239], v[16:19]
	v_mfma_f32_16x16x32_bf16 v[12:15], v[198:201], v[236:239], v[12:15]
	v_mfma_f32_16x16x32_bf16 v[8:11], v[190:193], v[244:247], v[8:11]
	v_mfma_f32_16x16x32_bf16 v[4:7], v[198:201], v[244:247], v[4:7]
	s_barrier
	s_add_i32 s20, 0, 0x18000
	v_add_u32_e32 v2, s20, v170
	s_add_i32 s21, 0, 0x1c000
	ds_read_b128 v[136:139], v2
	ds_read_b128 v[140:143], v2 offset:1024
	ds_read_b128 v[144:147], v2 offset:2048
	ds_read_b128 v[182:185], v2 offset:3072
	v_add_u32_e32 v2, s21, v170
	ds_read_b128 v[186:189], v2
	ds_read_b128 v[190:193], v2 offset:1024
	ds_read_b128 v[194:197], v2 offset:2048
	ds_read_b128 v[198:201], v2 offset:3072
	s_mov_b32 m0, s22
	ds_read_b128 v[202:205], v177 offset:32768
	ds_read_b128 v[208:211], v177 offset:33792
	ds_read_b128 v[224:227], v177 offset:34816
	ds_read_b128 v[228:231], v177 offset:35840
	ds_read_b128 v[232:235], v177 offset:36864
	ds_read_b128 v[236:239], v177 offset:37888
	ds_read_b128 v[240:243], v177 offset:38912
	ds_read_b128 v[244:247], v177 offset:39936
	global_load_lds_dwordx4 v153, s[14:15]
	s_mov_b32 m0, s23
	s_nop 0
	global_load_lds_dwordx4 v155, s[14:15]
	s_waitcnt vmcnt(8)
	s_waitcnt lgkmcnt(0)
	s_barrier
	s_waitcnt lgkmcnt(0)
	v_mfma_f32_16x16x32_bf16 v[128:131], v[136:139], v[202:205], v[128:131]
	v_mfma_f32_16x16x32_bf16 v[124:127], v[144:147], v[202:205], v[124:127]
	v_mfma_f32_16x16x32_bf16 v[120:123], v[136:139], v[224:227], v[120:123]
	v_mfma_f32_16x16x32_bf16 v[116:119], v[144:147], v[224:227], v[116:119]
	v_mfma_f32_16x16x32_bf16 v[112:115], v[136:139], v[232:235], v[112:115]
	v_mfma_f32_16x16x32_bf16 v[108:111], v[144:147], v[232:235], v[108:111]
	v_mfma_f32_16x16x32_bf16 v[104:107], v[136:139], v[240:243], v[104:107]
	v_mfma_f32_16x16x32_bf16 v[100:103], v[144:147], v[240:243], v[100:103]
	v_mfma_f32_16x16x32_bf16 v[128:131], v[140:143], v[208:211], v[128:131]
	v_mfma_f32_16x16x32_bf16 v[124:127], v[182:185], v[208:211], v[124:127]
	v_mfma_f32_16x16x32_bf16 v[120:123], v[140:143], v[228:231], v[120:123]
	v_mfma_f32_16x16x32_bf16 v[116:119], v[182:185], v[228:231], v[116:119]
	v_mfma_f32_16x16x32_bf16 v[112:115], v[140:143], v[236:239], v[112:115]
	v_mfma_f32_16x16x32_bf16 v[108:111], v[182:185], v[236:239], v[108:111]
	v_mfma_f32_16x16x32_bf16 v[104:107], v[140:143], v[244:247], v[104:107]
	v_mfma_f32_16x16x32_bf16 v[100:103], v[182:185], v[244:247], v[100:103]
	v_mfma_f32_16x16x32_bf16 v[96:99], v[186:189], v[202:205], v[96:99]
	v_mfma_f32_16x16x32_bf16 v[92:95], v[194:197], v[202:205], v[92:95]
	v_mfma_f32_16x16x32_bf16 v[88:91], v[186:189], v[224:227], v[88:91]
	v_mfma_f32_16x16x32_bf16 v[84:87], v[194:197], v[224:227], v[84:87]
	v_mfma_f32_16x16x32_bf16 v[80:83], v[186:189], v[232:235], v[80:83]
	v_mfma_f32_16x16x32_bf16 v[76:79], v[194:197], v[232:235], v[76:79]
	v_mfma_f32_16x16x32_bf16 v[72:75], v[186:189], v[240:243], v[72:75]
	v_mfma_f32_16x16x32_bf16 v[68:71], v[194:197], v[240:243], v[68:71]
	v_mfma_f32_16x16x32_bf16 v[96:99], v[190:193], v[208:211], v[96:99]
	v_mfma_f32_16x16x32_bf16 v[92:95], v[198:201], v[208:211], v[92:95]
	v_mfma_f32_16x16x32_bf16 v[88:91], v[190:193], v[228:231], v[88:91]
	v_mfma_f32_16x16x32_bf16 v[84:87], v[198:201], v[228:231], v[84:87]
	v_mfma_f32_16x16x32_bf16 v[80:83], v[190:193], v[236:239], v[80:83]
	v_mfma_f32_16x16x32_bf16 v[76:79], v[198:201], v[236:239], v[76:79]
	v_mfma_f32_16x16x32_bf16 v[72:75], v[190:193], v[244:247], v[72:75]
	v_mfma_f32_16x16x32_bf16 v[68:71], v[198:201], v[244:247], v[68:71]
	s_barrier
; #define PG8_STAGE(bufoff, gbase, voff) do { _Pragma("unroll") for (int _i = 0; _i < 2; ++_i) \
;         __builtin_amdgcn_global_load_lds((const unsigned*)((const char*)(gbase) + (voff)[_i]), (PG8_LAS unsigned*)(lds + (bufoff) + ldsw + _i * 8192), 16, 0, 0); } while (0)
; #define PG8_STAGE_G(bufoff, kb, g) do { _Pragma("unroll") for (int _i = 0; _i < 2; ++_i) \
;         __builtin_amdgcn_global_load_lds((const unsigned*)(gA + (size_t)(kb) + (g)[_i]), (PG8_LAS unsigned*)(lds + (bufoff) + ldsw + _i * 8192), 16, 0, 0); } while (0)
; #define PG8_LDA(dst, b, h) do { _Pragma("unroll") for (int m = 0; m < 4; ++m) _Pragma("unroll") for (int k = 0; k < 2; ++k) dst[m][k] = *(const PG8_LAS bf16x8*)(lds + PG8_SA(b, h) + aoff + m * 2048 + k * 1024); } while (0)
; #define PG8_MMA(ai, bj, At, Bt) do { __builtin_amdgcn_s_setprio(1); _Pragma("unroll") for (int m = 0; m < 4; ++m) _Pragma("unroll") for (int n = 0; n < 2; ++n) _Pragma("unroll") for (int k = 0; k < 2; ++k) \
;         acc[ai][bj][m][n] = __builtin_amdgcn_mfma_f32_16x16x32_bf16(Bt[n][k], At[m][k], acc[ai][bj][m][n], 0, 0, 0); __builtin_amdgcn_s_setprio(0); } while (0)
; #define PG8_WAIT_V(n) asm volatile("s_waitcnt vmcnt(" #n ")" ::: "memory")
; #define PG8_WAIT_L(n) asm volatile("s_waitcnt lgkmcnt(" #n ")" ::: "memory")
; #define PG8_BAR __builtin_amdgcn_s_barrier()
; #define PG8_SCHED __builtin_amdgcn_sched_barrier(0)
; template <class Epi, class Sched, bool ALIGN_EPI = false, bool SP2 = false, bool GATHER = false, bool HALFM = false>
; __device__ __forceinline__ void gemm_phase(PG8_LAS unsigned char* lds, const int Kdim, const Sched& S, const Epi& E) {
;     ...
;         for (int t = 0; t < nt; t += 2) {
;     ...
;             if constexpr (!HALFM) PG8_LDA(At, 1, 1); PG8_STAGE(PG8_SB(1, 0), b3, voffB); PG8_STAGE(PG8_SB(1, 1), b3 + hstep, voffB); if constexpr (GATHER) PG8_STAGE_G(PG8_SA(1, 0), kb2 + kstep, s0); else PG8_STAGE(PG8_SA(1, 0), a3, voffA);
;             PG8_WAIT_V(8); PG8_WAIT_L(0); PG8_BAR; if constexpr (!HALFM) { PG8_MMA(1, 0, At, B0); PG8_MMA(1, 1, At, B1); } PG8_BAR; PG8_SCHED;
	s_add_i32 s14, s20, s8
	v_lshl_add_u64 v[220:221], v[220:221], 0, s[34:35]
	s_mov_b32 m0, s14
	ds_read_b128 v[202:205], v177 offset:49152
	ds_read_b128 v[208:211], v177 offset:50176
	ds_read_b128 v[224:227], v177 offset:51200
	ds_read_b128 v[228:231], v177 offset:52224
	ds_read_b128 v[232:235], v177 offset:53248
	ds_read_b128 v[236:239], v177 offset:54272
	ds_read_b128 v[240:243], v177 offset:55296
	ds_read_b128 v[244:247], v177 offset:56320
	global_load_lds_dwordx4 v[220:221], off
	s_add_i32 m0, s14, 0x2000
	s_add_u32 s4, s4, 0x40080
	v_lshl_add_u64 v[216:217], v[216:217], 0, s[34:35]
	s_addc_u32 s5, s5, 0
	s_add_i32 s14, s21, s8
	global_load_lds_dwordx4 v[216:217], off
	v_lshl_add_u64 v[216:217], s[4:5], 0, v[156:157]
	s_mov_b32 m0, s14
	v_lshl_add_u64 v[160:161], v[160:161], 0, s[34:35]
	global_load_lds_dwordx4 v[216:217], off
	v_lshl_add_u64 v[216:217], s[4:5], 0, v[158:159]
	s_add_i32 m0, s14, 0x2000
	s_nop 0
	global_load_lds_dwordx4 v[216:217], off
	v_lshl_add_u64 v[216:217], v[218:219], 0, s[34:35]
	s_mov_b32 m0, s50
	s_nop 0
	global_load_lds_dwordx4 v[216:217], off
	s_mov_b32 m0, s51
	s_nop 0
	global_load_lds_dwordx4 v[160:161], off
	s_waitcnt vmcnt(8)
	s_waitcnt lgkmcnt(0)
	s_barrier
	s_waitcnt lgkmcnt(0)
	v_mfma_f32_16x16x32_bf16 v[64:67], v[136:139], v[202:205], v[64:67]
	v_mfma_f32_16x16x32_bf16 v[60:63], v[144:147], v[202:205], v[60:63]
	v_mfma_f32_16x16x32_bf16 v[56:59], v[136:139], v[224:227], v[56:59]
	v_mfma_f32_16x16x32_bf16 v[52:55], v[144:147], v[224:227], v[52:55]
	v_mfma_f32_16x16x32_bf16 v[48:51], v[136:139], v[232:235], v[48:51]
	v_mfma_f32_16x16x32_bf16 v[44:47], v[144:147], v[232:235], v[44:47]
	v_mfma_f32_16x16x32_bf16 v[40:43], v[136:139], v[240:243], v[40:43]
	v_mfma_f32_16x16x32_bf16 v[36:39], v[144:147], v[240:243], v[36:39]
	v_mfma_f32_16x16x32_bf16 v[64:67], v[140:143], v[208:211], v[64:67]
	v_mfma_f32_16x16x32_bf16 v[60:63], v[182:185], v[208:211], v[60:63]
	v_mfma_f32_16x16x32_bf16 v[56:59], v[140:143], v[228:231], v[56:59]
	v_mfma_f32_16x16x32_bf16 v[52:55], v[182:185], v[228:231], v[52:55]
	v_mfma_f32_16x16x32_bf16 v[48:51], v[140:143], v[236:239], v[48:51]
	v_mfma_f32_16x16x32_bf16 v[44:47], v[182:185], v[236:239], v[44:47]
	v_mfma_f32_16x16x32_bf16 v[40:43], v[140:143], v[244:247], v[40:43]
	v_mfma_f32_16x16x32_bf16 v[36:39], v[182:185], v[244:247], v[36:39]
	v_mfma_f32_16x16x32_bf16 v[32:35], v[186:189], v[202:205], v[32:35]
	v_mfma_f32_16x16x32_bf16 v[28:31], v[194:197], v[202:205], v[28:31]
	v_mfma_f32_16x16x32_bf16 v[24:27], v[186:189], v[224:227], v[24:27]
	v_mfma_f32_16x16x32_bf16 v[20:23], v[194:197], v[224:227], v[20:23]
	v_mfma_f32_16x16x32_bf16 v[16:19], v[186:189], v[232:235], v[16:19]
	v_mfma_f32_16x16x32_bf16 v[12:15], v[194:197], v[232:235], v[12:15]
	v_mfma_f32_16x16x32_bf16 v[8:11], v[186:189], v[240:243], v[8:11]
	v_mfma_f32_16x16x32_bf16 v[4:7], v[194:197], v[240:243], v[4:7]
	v_mfma_f32_16x16x32_bf16 v[32:35], v[190:193], v[208:211], v[32:35]
	v_mfma_f32_16x16x32_bf16 v[28:31], v[198:201], v[208:211], v[28:31]
	v_mfma_f32_16x16x32_bf16 v[24:27], v[190:193], v[228:231], v[24:27]
	v_mfma_f32_16x16x32_bf16 v[20:23], v[198:201], v[228:231], v[20:23]
	v_mfma_f32_16x16x32_bf16 v[16:19], v[190:193], v[236:239], v[16:19]
	v_mfma_f32_16x16x32_bf16 v[12:15], v[198:201], v[236:239], v[12:15]
	v_mfma_f32_16x16x32_bf16 v[8:11], v[190:193], v[244:247], v[8:11]
	v_mfma_f32_16x16x32_bf16 v[4:7], v[198:201], v[244:247], v[4:7]
	s_barrier
	s_add_i32 s83, s83, 2
	s_cmp_gt_u32 s83, 13
	s_mov_b64 s[14:15], s[24:25]
	s_cbranch_scc0 .LBB0_1716
	s_setprio 0
	s_and_b64 vcc, exec, s[6:7]
	s_cbranch_vccz .LBB0_1719
	s_barrier

; #define PG8_STAGE(bufoff, gbase, voff) do { _Pragma("unroll") for (int _i = 0; _i < 2; ++_i) \
;         __builtin_amdgcn_global_load_lds((const unsigned*)((const char*)(gbase) + (voff)[_i]), (PG8_LAS unsigned*)(lds + (bufoff) + ldsw + _i * 8192), 16, 0, 0); } while (0)
; #define PG8_STAGE_G(bufoff, kb, g) do { _Pragma("unroll") for (int _i = 0; _i < 2; ++_i) \
;         __builtin_amdgcn_global_load_lds((const unsigned*)(gA + (size_t)(kb) + (g)[_i]), (PG8_LAS unsigned*)(lds + (bufoff) + ldsw + _i * 8192), 16, 0, 0); } while (0)
; #define PG8_LDA(dst, b, h) do { _Pragma("unroll") for (int m = 0; m < 4; ++m) _Pragma("unroll") for (int k = 0; k < 2; ++k) dst[m][k] = *(const PG8_LAS bf16x8*)(lds + PG8_SA(b, h) + aoff + m * 2048 + k * 1024); } while (0)
; #define PG8_LDB(dst, b, h) do { _Pragma("unroll") for (int n = 0; n < 2; ++n) _Pragma("unroll") for (int k = 0; k < 2; ++k) dst[n][k] = *(const PG8_LAS bf16x8*)(lds + PG8_SB(b, h) + boff + n * 2048 + k * 1024); } while (0)
; #define PG8_MMA(ai, bj, At, Bt) do { __builtin_amdgcn_s_setprio(1); _Pragma("unroll") for (int m = 0; m < 4; ++m) _Pragma("unroll") for (int n = 0; n < 2; ++n) _Pragma("unroll") for (int k = 0; k < 2; ++k) \
;         acc[ai][bj][m][n] = __builtin_amdgcn_mfma_f32_16x16x32_bf16(Bt[n][k], At[m][k], acc[ai][bj][m][n], 0, 0, 0); __builtin_amdgcn_s_setprio(0); } while (0)
; #define PG8_WAIT_V(n) asm volatile("s_waitcnt vmcnt(" #n ")" ::: "memory")
; template <class Epi, class Sched, bool ALIGN_EPI = false, bool SP2 = false, bool GATHER = false, bool HALFM = false>
; __device__ __forceinline__ void gemm_phase(PG8_LAS unsigned char* lds, const int Kdim, const Sched& S, const Epi& E) {
;     ...
;             PG8_LDB(B0, 0, 0); PG8_LDB(B1, 0, 1); PG8_SCHED; PG8_LDA(At, 0, 0); if constexpr (GATHER) PG8_STAGE_G(PG8_SA(1, 1), (size_t)(t + 1) * kstep, gc[1]); else PG8_STAGE(PG8_SA(1, 1), a1 + hstep, voffA);
;             PG8_WAIT_V(8); PG8_WAIT_L(0); PG8_BAR; PG8_MMA(0, 0, At, B0); PG8_MMA(0, 1, At, B1); PG8_BAR; PG8_SCHED;
;             if constexpr (!HALFM) PG8_LDA(At, 0, 1); PG8_STAGE(PG8_SB(0, 0), b2, voffB); PG8_STAGE(PG8_SB(0, 1), b2 + hstep, voffB); if constexpr (GATHER) PG8_STAGE_G(PG8_SA(0, 0), kb2, s0); else PG8_STAGE(PG8_SA(0, 0), a2, voffA);
;             PG8_WAIT_V(8); PG8_WAIT_L(0); PG8_BAR; if constexpr (!HALFM) { PG8_MMA(1, 0, At, B0); PG8_MMA(1, 1, At, B1); } PG8_BAR; PG8_SCHED;
.Ldn_prio_done:
.LBB0_1817:
	s_add_u32 s4, s44, 0xfffc0080
	s_addc_u32 s5, s45, -1
	s_add_i32 s20, 0, 0x10000
	s_cmp_eq_u32 s57, 12
	s_cselect_b32 s25, s17, s5
	s_cselect_b32 s24, s36, s4
	s_cselect_b32 s5, s53, s56
	s_cselect_b32 s4, s54, s55
	s_add_i32 s33, 0, 0x14000
	v_add_u32_e32 v112, s20, v160
	v_add_u32_e32 v158, s33, v160
	ds_read_b128 v[100:103], v112
	ds_read_b128 v[104:107], v112 offset:1024
	ds_read_b128 v[108:111], v112 offset:2048
	ds_read_b128 v[112:115], v112 offset:3072
	ds_read_b128 v[170:173], v158
	ds_read_b128 v[174:177], v158 offset:1024
	ds_read_b128 v[178:181], v158 offset:2048
	ds_read_b128 v[182:185], v158 offset:3072
	v_lshl_add_u64 v[158:159], s[44:45], 0, v[154:155]
	s_add_i32 m0, s7, 0xc000
	ds_read_b128 v[186:189], v169
	ds_read_b128 v[190:193], v169 offset:1024
	ds_read_b128 v[194:197], v169 offset:2048
	ds_read_b128 v[198:201], v169 offset:3072
	ds_read_b128 v[202:205], v169 offset:4096
	ds_read_b128 v[208:211], v169 offset:5120
	ds_read_b128 v[224:227], v169 offset:6144
	ds_read_b128 v[228:231], v169 offset:7168
	global_load_lds_dwordx4 v[158:159], off
	v_lshl_add_u64 v[158:159], s[44:45], 0, v[156:157]
	s_add_i32 m0, s7, 0xe000
	s_nop 0
	global_load_lds_dwordx4 v[158:159], off
	s_waitcnt vmcnt(8)
	s_waitcnt lgkmcnt(0)
	s_barrier
	s_waitcnt lgkmcnt(0)
	v_mfma_f32_16x16x32_bf16 v[144:147], v[100:103], v[186:189], v[144:147]
	v_mfma_f32_16x16x32_bf16 v[140:143], v[108:111], v[186:189], v[140:143]
	v_mfma_f32_16x16x32_bf16 v[128:131], v[100:103], v[194:197], v[128:131]
	v_mfma_f32_16x16x32_bf16 v[124:127], v[108:111], v[194:197], v[124:127]
	v_mfma_f32_16x16x32_bf16 v[96:99], v[100:103], v[202:205], v[96:99]
	v_mfma_f32_16x16x32_bf16 v[92:95], v[108:111], v[202:205], v[92:95]
	v_mfma_f32_16x16x32_bf16 v[80:83], v[100:103], v[224:227], v[80:83]
	v_mfma_f32_16x16x32_bf16 v[76:79], v[108:111], v[224:227], v[76:79]
	v_mfma_f32_16x16x32_bf16 v[144:147], v[104:107], v[190:193], v[144:147]
	v_mfma_f32_16x16x32_bf16 v[140:143], v[112:115], v[190:193], v[140:143]
	v_mfma_f32_16x16x32_bf16 v[128:131], v[104:107], v[198:201], v[128:131]
	v_mfma_f32_16x16x32_bf16 v[124:127], v[112:115], v[198:201], v[124:127]
	v_mfma_f32_16x16x32_bf16 v[96:99], v[104:107], v[208:211], v[96:99]
	v_mfma_f32_16x16x32_bf16 v[92:95], v[112:115], v[208:211], v[92:95]
	v_mfma_f32_16x16x32_bf16 v[80:83], v[104:107], v[228:231], v[80:83]
	v_mfma_f32_16x16x32_bf16 v[76:79], v[112:115], v[228:231], v[76:79]
	v_mfma_f32_16x16x32_bf16 v[136:139], v[170:173], v[186:189], v[136:139]
	v_mfma_f32_16x16x32_bf16 v[132:135], v[178:181], v[186:189], v[132:135]
	v_mfma_f32_16x16x32_bf16 v[120:123], v[170:173], v[194:197], v[120:123]
	v_mfma_f32_16x16x32_bf16 v[116:119], v[178:181], v[194:197], v[116:119]
	v_mfma_f32_16x16x32_bf16 v[88:91], v[170:173], v[202:205], v[88:91]
	v_mfma_f32_16x16x32_bf16 v[84:87], v[178:181], v[202:205], v[84:87]
	v_mfma_f32_16x16x32_bf16 v[72:75], v[170:173], v[224:227], v[72:75]
	v_mfma_f32_16x16x32_bf16 v[68:71], v[178:181], v[224:227], v[68:71]
	v_mfma_f32_16x16x32_bf16 v[136:139], v[174:177], v[190:193], v[136:139]
	v_mfma_f32_16x16x32_bf16 v[132:135], v[182:185], v[190:193], v[132:135]
	v_mfma_f32_16x16x32_bf16 v[120:123], v[174:177], v[198:201], v[120:123]
	v_mfma_f32_16x16x32_bf16 v[116:119], v[182:185], v[198:201], v[116:119]
	v_mfma_f32_16x16x32_bf16 v[88:91], v[174:177], v[208:211], v[88:91]
	v_mfma_f32_16x16x32_bf16 v[84:87], v[182:185], v[208:211], v[84:87]
	v_mfma_f32_16x16x32_bf16 v[72:75], v[174:177], v[228:231], v[72:75]
	v_mfma_f32_16x16x32_bf16 v[68:71], v[182:185], v[228:231], v[68:71]
	s_barrier
	s_add_i32 s20, s20, s13
	v_lshl_add_u64 v[158:159], s[4:5], 0, v[2:3]
	s_mov_b32 m0, s20
	ds_read_b128 v[186:189], v169 offset:16384
	ds_read_b128 v[190:193], v169 offset:17408
	ds_read_b128 v[194:197], v169 offset:18432
	ds_read_b128 v[198:201], v169 offset:19456
	ds_read_b128 v[202:205], v169 offset:20480
	ds_read_b128 v[208:211], v169 offset:21504
	ds_read_b128 v[224:227], v169 offset:22528
	ds_read_b128 v[228:231], v169 offset:23552
	global_load_lds_dwordx4 v[158:159], off
	s_add_i32 m0, s20, 0x2000
	s_add_u32 s20, s4, 0x40000
	v_lshl_add_u64 v[216:217], s[4:5], 0, v[148:149]
	s_addc_u32 s21, s5, 0
	s_add_i32 s33, s33, s13
	global_load_lds_dwordx4 v[216:217], off
	v_lshl_add_u64 v[218:219], s[20:21], 0, v[2:3]
	s_mov_b32 m0, s33
	v_lshl_add_u64 v[220:221], s[24:25], 0, v[150:151]
	global_load_lds_dwordx4 v[218:219], off
	v_lshl_add_u64 v[218:219], s[20:21], 0, v[148:149]
	s_add_i32 m0, s33, 0x2000
	s_nop 0
	global_load_lds_dwordx4 v[218:219], off
	v_lshl_add_u64 v[218:219], s[24:25], 0, v[152:153]
	s_mov_b32 m0, s7
	s_nop 0
	global_load_lds_dwordx4 v[218:219], off
	s_mov_b32 m0, s22
	s_nop 0
	global_load_lds_dwordx4 v[220:221], off
	s_waitcnt vmcnt(8)
	s_waitcnt lgkmcnt(0)
	s_barrier
; #define PG8_STAGE(bufoff, gbase, voff) do { _Pragma("unroll") for (int _i = 0; _i < 2; ++_i) \
;         __builtin_amdgcn_global_load_lds((const unsigned*)((const char*)(gbase) + (voff)[_i]), (PG8_LAS unsigned*)(lds + (bufoff) + ldsw + _i * 8192), 16, 0, 0); } while (0)
; #define PG8_STAGE_G(bufoff, kb, g) do { _Pragma("unroll") for (int _i = 0; _i < 2; ++_i) \
;         __builtin_amdgcn_global_load_lds((const unsigned*)(gA + (size_t)(kb) + (g)[_i]), (PG8_LAS unsigned*)(lds + (bufoff) + ldsw + _i * 8192), 16, 0, 0); } while (0)
; #define PG8_LDA(dst, b, h) do { _Pragma("unroll") for (int m = 0; m < 4; ++m) _Pragma("unroll") for (int k = 0; k < 2; ++k) dst[m][k] = *(const PG8_LAS bf16x8*)(lds + PG8_SA(b, h) + aoff + m * 2048 + k * 1024); } while (0)
; #define PG8_LDB(dst, b, h) do { _Pragma("unroll") for (int n = 0; n < 2; ++n) _Pragma("unroll") for (int k = 0; k < 2; ++k) dst[n][k] = *(const PG8_LAS bf16x8*)(lds + PG8_SB(b, h) + boff + n * 2048 + k * 1024); } while (0)
; #define PG8_MMA(ai, bj, At, Bt) do { __builtin_amdgcn_s_setprio(1); _Pragma("unroll") for (int m = 0; m < 4; ++m) _Pragma("unroll") for (int n = 0; n < 2; ++n) _Pragma("unroll") for (int k = 0; k < 2; ++k) \
;         acc[ai][bj][m][n] = __builtin_amdgcn_mfma_f32_16x16x32_bf16(Bt[n][k], At[m][k], acc[ai][bj][m][n], 0, 0, 0); __builtin_amdgcn_s_setprio(0); } while (0)
; #define PG8_WAIT_V(n) asm volatile("s_waitcnt vmcnt(" #n ")" ::: "memory")
; #define PG8_WAIT_L(n) asm volatile("s_waitcnt lgkmcnt(" #n ")" ::: "memory")
; #define PG8_BAR __builtin_amdgcn_s_barrier()
; #define PG8_SCHED __builtin_amdgcn_sched_barrier(0)
; template <class Epi, class Sched, bool ALIGN_EPI = false, bool SP2 = false, bool GATHER = false, bool HALFM = false>
; __device__ __forceinline__ void gemm_phase(PG8_LAS unsigned char* lds, const int Kdim, const Sched& S, const Epi& E) {
;     ...
;             PG8_WAIT_V(8); PG8_WAIT_L(0); PG8_BAR; if constexpr (!HALFM) { PG8_MMA(1, 0, At, B0); PG8_MMA(1, 1, At, B1); } PG8_BAR; PG8_SCHED;
;             PG8_LDB(B0, 1, 0); PG8_LDB(B1, 1, 1); PG8_SCHED; PG8_LDA(At, 1, 0); if constexpr (GATHER) PG8_STAGE_G(PG8_SA(0, 1), kb2, s1); else PG8_STAGE(PG8_SA(0, 1), a2 + hstep, voffA);
;             PG8_WAIT_V(8); PG8_WAIT_L(0); PG8_BAR; PG8_MMA(0, 0, At, B0); PG8_MMA(0, 1, At, B1); PG8_BAR; PG8_SCHED;
	s_waitcnt lgkmcnt(0)
	v_mfma_f32_16x16x32_bf16 v[64:67], v[100:103], v[186:189], v[64:67]
	v_mfma_f32_16x16x32_bf16 v[60:63], v[108:111], v[186:189], v[60:63]
	v_mfma_f32_16x16x32_bf16 v[52:55], v[100:103], v[194:197], v[52:55]
	v_mfma_f32_16x16x32_bf16 v[44:47], v[108:111], v[194:197], v[44:47]
	v_mfma_f32_16x16x32_bf16 v[36:39], v[100:103], v[202:205], v[36:39]
	v_mfma_f32_16x16x32_bf16 v[28:31], v[108:111], v[202:205], v[28:31]
	v_mfma_f32_16x16x32_bf16 v[20:23], v[100:103], v[224:227], v[20:23]
	v_mfma_f32_16x16x32_bf16 v[12:15], v[108:111], v[224:227], v[12:15]
	v_mfma_f32_16x16x32_bf16 v[64:67], v[104:107], v[190:193], v[64:67]
	v_mfma_f32_16x16x32_bf16 v[60:63], v[112:115], v[190:193], v[60:63]
	v_mfma_f32_16x16x32_bf16 v[52:55], v[104:107], v[198:201], v[52:55]
	v_mfma_f32_16x16x32_bf16 v[44:47], v[112:115], v[198:201], v[44:47]
	v_mfma_f32_16x16x32_bf16 v[36:39], v[104:107], v[208:211], v[36:39]
	v_mfma_f32_16x16x32_bf16 v[28:31], v[112:115], v[208:211], v[28:31]
	v_mfma_f32_16x16x32_bf16 v[20:23], v[104:107], v[228:231], v[20:23]
	v_mfma_f32_16x16x32_bf16 v[12:15], v[112:115], v[228:231], v[12:15]
	v_mfma_f32_16x16x32_bf16 v[56:59], v[170:173], v[186:189], v[56:59]
	v_mfma_f32_16x16x32_bf16 v[48:51], v[178:181], v[186:189], v[48:51]
	v_mfma_f32_16x16x32_bf16 v[40:43], v[170:173], v[194:197], v[40:43]
	v_mfma_f32_16x16x32_bf16 v[32:35], v[178:181], v[194:197], v[32:35]
	v_mfma_f32_16x16x32_bf16 v[24:27], v[170:173], v[202:205], v[24:27]
	v_mfma_f32_16x16x32_bf16 v[16:19], v[178:181], v[202:205], v[16:19]
	v_mfma_f32_16x16x32_bf16 v[8:11], v[170:173], v[224:227], v[8:11]
	v_mfma_f32_16x16x32_bf16 v[4:7], v[178:181], v[224:227], v[4:7]
	v_mfma_f32_16x16x32_bf16 v[56:59], v[174:177], v[190:193], v[56:59]
	v_mfma_f32_16x16x32_bf16 v[48:51], v[182:185], v[190:193], v[48:51]
	v_mfma_f32_16x16x32_bf16 v[40:43], v[174:177], v[198:201], v[40:43]
	v_mfma_f32_16x16x32_bf16 v[32:35], v[182:185], v[198:201], v[32:35]
	v_mfma_f32_16x16x32_bf16 v[24:27], v[174:177], v[208:211], v[24:27]
	v_mfma_f32_16x16x32_bf16 v[16:19], v[182:185], v[208:211], v[16:19]
	v_mfma_f32_16x16x32_bf16 v[8:11], v[174:177], v[228:231], v[8:11]
	v_mfma_f32_16x16x32_bf16 v[4:7], v[182:185], v[228:231], v[4:7]
	s_barrier
	s_add_i32 s33, 0, 0x18000
	s_add_i32 s76, 0, 0x1c000
	v_add_u32_e32 v112, s33, v160
	v_add_u32_e32 v182, s76, v160
	ds_read_b128 v[100:103], v112
	ds_read_b128 v[104:107], v112 offset:1024
	ds_read_b128 v[108:111], v112 offset:2048
	ds_read_b128 v[112:115], v112 offset:3072
	ds_read_b128 v[170:173], v182
	ds_read_b128 v[174:177], v182 offset:1024
	ds_read_b128 v[178:181], v182 offset:2048
	ds_read_b128 v[182:185], v182 offset:3072
	s_add_u32 s20, s24, 0x40000
	s_addc_u32 s21, s25, 0
	s_mov_b32 m0, s23
	v_lshl_add_u64 v[232:233], s[20:21], 0, v[152:153]
	ds_read_b128 v[186:189], v169 offset:32768
	ds_read_b128 v[190:193], v169 offset:33792
	ds_read_b128 v[194:197], v169 offset:34816
	ds_read_b128 v[198:201], v169 offset:35840
	ds_read_b128 v[202:205], v169 offset:36864
	ds_read_b128 v[208:211], v169 offset:37888
	ds_read_b128 v[224:227], v169 offset:38912
	ds_read_b128 v[228:231], v169 offset:39936
	global_load_lds_dwordx4 v[232:233], off
	v_lshl_add_u64 v[232:233], s[20:21], 0, v[150:151]
	s_mov_b32 m0, s26
	s_nop 0
	global_load_lds_dwordx4 v[232:233], off
	s_waitcnt vmcnt(8)
	s_waitcnt lgkmcnt(0)
	s_barrier
	s_waitcnt lgkmcnt(0)
	v_mfma_f32_16x16x32_bf16 v[144:147], v[100:103], v[186:189], v[144:147]
	v_mfma_f32_16x16x32_bf16 v[140:143], v[108:111], v[186:189], v[140:143]
	v_mfma_f32_16x16x32_bf16 v[128:131], v[100:103], v[194:197], v[128:131]
	v_mfma_f32_16x16x32_bf16 v[124:127], v[108:111], v[194:197], v[124:127]
	v_mfma_f32_16x16x32_bf16 v[96:99], v[100:103], v[202:205], v[96:99]
	v_mfma_f32_16x16x32_bf16 v[92:95], v[108:111], v[202:205], v[92:95]
	v_mfma_f32_16x16x32_bf16 v[80:83], v[100:103], v[224:227], v[80:83]
	v_mfma_f32_16x16x32_bf16 v[76:79], v[108:111], v[224:227], v[76:79]
	v_mfma_f32_16x16x32_bf16 v[144:147], v[104:107], v[190:193], v[144:147]
	v_mfma_f32_16x16x32_bf16 v[140:143], v[112:115], v[190:193], v[140:143]
	v_mfma_f32_16x16x32_bf16 v[128:131], v[104:107], v[198:201], v[128:131]
	v_mfma_f32_16x16x32_bf16 v[124:127], v[112:115], v[198:201], v[124:127]
	v_mfma_f32_16x16x32_bf16 v[96:99], v[104:107], v[208:211], v[96:99]
	v_mfma_f32_16x16x32_bf16 v[92:95], v[112:115], v[208:211], v[92:95]
	v_mfma_f32_16x16x32_bf16 v[80:83], v[104:107], v[228:231], v[80:83]
	v_mfma_f32_16x16x32_bf16 v[76:79], v[112:115], v[228:231], v[76:79]
	v_mfma_f32_16x16x32_bf16 v[136:139], v[170:173], v[186:189], v[136:139]
	v_mfma_f32_16x16x32_bf16 v[132:135], v[178:181], v[186:189], v[132:135]
	v_mfma_f32_16x16x32_bf16 v[120:123], v[170:173], v[194:197], v[120:123]
	v_mfma_f32_16x16x32_bf16 v[116:119], v[178:181], v[194:197], v[116:119]
	v_mfma_f32_16x16x32_bf16 v[88:91], v[170:173], v[202:205], v[88:91]
	v_mfma_f32_16x16x32_bf16 v[84:87], v[178:181], v[202:205], v[84:87]
	v_mfma_f32_16x16x32_bf16 v[72:75], v[170:173], v[224:227], v[72:75]
	v_mfma_f32_16x16x32_bf16 v[68:71], v[178:181], v[224:227], v[68:71]
	v_mfma_f32_16x16x32_bf16 v[136:139], v[174:177], v[190:193], v[136:139]
	v_mfma_f32_16x16x32_bf16 v[132:135], v[182:185], v[190:193], v[132:135]
	v_mfma_f32_16x16x32_bf16 v[120:123], v[174:177], v[198:201], v[120:123]
	v_mfma_f32_16x16x32_bf16 v[116:119], v[182:185], v[198:201], v[116:119]
	v_mfma_f32_16x16x32_bf16 v[88:91], v[174:177], v[208:211], v[88:91]
	v_mfma_f32_16x16x32_bf16 v[84:87], v[182:185], v[208:211], v[84:87]
	v_mfma_f32_16x16x32_bf16 v[72:75], v[174:177], v[228:231], v[72:75]
	v_mfma_f32_16x16x32_bf16 v[68:71], v[182:185], v[228:231], v[68:71]
	s_barrier
; #define PG8_STAGE(bufoff, gbase, voff) do { _Pragma("unroll") for (int _i = 0; _i < 2; ++_i) \
;         __builtin_amdgcn_global_load_lds((const unsigned*)((const char*)(gbase) + (voff)[_i]), (PG8_LAS unsigned*)(lds + (bufoff) + ldsw + _i * 8192), 16, 0, 0); } while (0)
; #define PG8_STAGE_G(bufoff, kb, g) do { _Pragma("unroll") for (int _i = 0; _i < 2; ++_i) \
;         __builtin_amdgcn_global_load_lds((const unsigned*)(gA + (size_t)(kb) + (g)[_i]), (PG8_LAS unsigned*)(lds + (bufoff) + ldsw + _i * 8192), 16, 0, 0); } while (0)
; #define PG8_LDA(dst, b, h) do { _Pragma("unroll") for (int m = 0; m < 4; ++m) _Pragma("unroll") for (int k = 0; k < 2; ++k) dst[m][k] = *(const PG8_LAS bf16x8*)(lds + PG8_SA(b, h) + aoff + m * 2048 + k * 1024); } while (0)
; #define PG8_MMA(ai, bj, At, Bt) do { __builtin_amdgcn_s_setprio(1); _Pragma("unroll") for (int m = 0; m < 4; ++m) _Pragma("unroll") for (int n = 0; n < 2; ++n) _Pragma("unroll") for (int k = 0; k < 2; ++k) \
;         acc[ai][bj][m][n] = __builtin_amdgcn_mfma_f32_16x16x32_bf16(Bt[n][k], At[m][k], acc[ai][bj][m][n], 0, 0, 0); __builtin_amdgcn_s_setprio(0); } while (0)
; #define PG8_WAIT_V(n) asm volatile("s_waitcnt vmcnt(" #n ")" ::: "memory")
; #define PG8_WAIT_L(n) asm volatile("s_waitcnt lgkmcnt(" #n ")" ::: "memory")
; #define PG8_BAR __builtin_amdgcn_s_barrier()
; #define PG8_SCHED __builtin_amdgcn_sched_barrier(0)
; template <class Epi, class Sched, bool ALIGN_EPI = false, bool SP2 = false, bool GATHER = false, bool HALFM = false>
; __device__ __forceinline__ void gemm_phase(PG8_LAS unsigned char* lds, const int Kdim, const Sched& S, const Epi& E) {
;     ...
;             if constexpr (!HALFM) PG8_LDA(At, 1, 1); PG8_STAGE(PG8_SB(1, 0), b3, voffB); PG8_STAGE(PG8_SB(1, 1), b3 + hstep, voffB); if constexpr (GATHER) PG8_STAGE_G(PG8_SA(1, 0), kb2 + kstep, s0); else PG8_STAGE(PG8_SA(1, 0), a3, voffA);
;             PG8_WAIT_V(8); PG8_WAIT_L(0); PG8_BAR; if constexpr (!HALFM) { PG8_MMA(1, 0, At, B0); PG8_MMA(1, 1, At, B1); } PG8_BAR; PG8_SCHED;
	s_add_i32 s20, s33, s13
	v_lshl_add_u64 v[158:159], v[158:159], 0, s[34:35]
	s_mov_b32 m0, s20
	ds_read_b128 v[186:189], v169 offset:49152
	ds_read_b128 v[190:193], v169 offset:50176
	ds_read_b128 v[194:197], v169 offset:51200
	ds_read_b128 v[198:201], v169 offset:52224
	ds_read_b128 v[202:205], v169 offset:53248
	ds_read_b128 v[208:211], v169 offset:54272
	ds_read_b128 v[224:227], v169 offset:55296
	ds_read_b128 v[228:231], v169 offset:56320
	global_load_lds_dwordx4 v[158:159], off
	s_add_i32 m0, s20, 0x2000
	s_add_u32 s4, s4, 0x40080
	v_lshl_add_u64 v[158:159], v[216:217], 0, s[34:35]
	s_addc_u32 s5, s5, 0
	s_add_i32 s20, s76, s13
	global_load_lds_dwordx4 v[158:159], off
	v_lshl_add_u64 v[158:159], s[4:5], 0, v[2:3]
	s_mov_b32 m0, s20
	s_nop 0
	global_load_lds_dwordx4 v[158:159], off
	v_lshl_add_u64 v[158:159], s[4:5], 0, v[148:149]
	s_add_i32 m0, s20, 0x2000
	s_nop 0
	global_load_lds_dwordx4 v[158:159], off
	v_lshl_add_u64 v[158:159], v[218:219], 0, s[34:35]
	s_mov_b32 m0, s46
	s_nop 0
	global_load_lds_dwordx4 v[158:159], off
	v_lshl_add_u64 v[158:159], v[220:221], 0, s[34:35]
	s_mov_b32 m0, s47
	s_nop 0
	global_load_lds_dwordx4 v[158:159], off
	s_waitcnt vmcnt(8)
	s_waitcnt lgkmcnt(0)
	s_barrier
	s_waitcnt lgkmcnt(0)
	v_mfma_f32_16x16x32_bf16 v[64:67], v[100:103], v[186:189], v[64:67]
	v_mfma_f32_16x16x32_bf16 v[60:63], v[108:111], v[186:189], v[60:63]
	v_mfma_f32_16x16x32_bf16 v[52:55], v[100:103], v[194:197], v[52:55]
	v_mfma_f32_16x16x32_bf16 v[44:47], v[108:111], v[194:197], v[44:47]
	v_mfma_f32_16x16x32_bf16 v[36:39], v[100:103], v[202:205], v[36:39]
	v_mfma_f32_16x16x32_bf16 v[28:31], v[108:111], v[202:205], v[28:31]
	v_mfma_f32_16x16x32_bf16 v[20:23], v[100:103], v[224:227], v[20:23]
	v_mfma_f32_16x16x32_bf16 v[12:15], v[108:111], v[224:227], v[12:15]
	v_mfma_f32_16x16x32_bf16 v[64:67], v[104:107], v[190:193], v[64:67]
	v_mfma_f32_16x16x32_bf16 v[60:63], v[112:115], v[190:193], v[60:63]
	v_mfma_f32_16x16x32_bf16 v[52:55], v[104:107], v[198:201], v[52:55]
	v_mfma_f32_16x16x32_bf16 v[44:47], v[112:115], v[198:201], v[44:47]
	v_mfma_f32_16x16x32_bf16 v[36:39], v[104:107], v[208:211], v[36:39]
	v_mfma_f32_16x16x32_bf16 v[28:31], v[112:115], v[208:211], v[28:31]
	v_mfma_f32_16x16x32_bf16 v[20:23], v[104:107], v[228:231], v[20:23]
	v_mfma_f32_16x16x32_bf16 v[12:15], v[112:115], v[228:231], v[12:15]
	v_mfma_f32_16x16x32_bf16 v[56:59], v[170:173], v[186:189], v[56:59]
	v_mfma_f32_16x16x32_bf16 v[48:51], v[178:181], v[186:189], v[48:51]
	v_mfma_f32_16x16x32_bf16 v[40:43], v[170:173], v[194:197], v[40:43]
	v_mfma_f32_16x16x32_bf16 v[32:35], v[178:181], v[194:197], v[32:35]
	v_mfma_f32_16x16x32_bf16 v[24:27], v[170:173], v[202:205], v[24:27]
	v_mfma_f32_16x16x32_bf16 v[16:19], v[178:181], v[202:205], v[16:19]
	v_mfma_f32_16x16x32_bf16 v[8:11], v[170:173], v[224:227], v[8:11]
	v_mfma_f32_16x16x32_bf16 v[4:7], v[178:181], v[224:227], v[4:7]
	v_mfma_f32_16x16x32_bf16 v[56:59], v[174:177], v[190:193], v[56:59]
	v_mfma_f32_16x16x32_bf16 v[48:51], v[182:185], v[190:193], v[48:51]
	v_mfma_f32_16x16x32_bf16 v[40:43], v[174:177], v[198:201], v[40:43]
	v_mfma_f32_16x16x32_bf16 v[32:35], v[182:185], v[198:201], v[32:35]
	v_mfma_f32_16x16x32_bf16 v[24:27], v[174:177], v[208:211], v[24:27]
	v_mfma_f32_16x16x32_bf16 v[16:19], v[182:185], v[208:211], v[16:19]
	v_mfma_f32_16x16x32_bf16 v[8:11], v[174:177], v[228:231], v[8:11]
	v_mfma_f32_16x16x32_bf16 v[4:7], v[182:185], v[228:231], v[4:7]
	s_barrier
	s_add_i32 s57, s57, 2
	s_add_u32 s44, s44, 0x100
	s_addc_u32 s45, s45, 0
	s_add_u32 s55, s55, 0x100
	s_addc_u32 s56, s56, 0
	s_cmp_gt_u32 s57, 13
	s_cbranch_scc0 .LBB0_1817
	s_setprio 0
	s_and_b64 vcc, exec, s[14:15]
	s_cbranch_vccz .LBB0_1820
	s_barrier
